# baseline (speedup 1.0000x reference)
_Z8k_expertPKDF16_S0_PKfPcPiS0_S2_S2_S2_S2_PfS5_S4_S2_S2_S2_S2_S5_S2_S2_S2_:
	s_lshl_b32 s3, s2, 2
	s_load_dwordx8 s[8:15], s[0:1], 0x88
	s_load_dwordx2 s[70:71], s[0:1], 0x0
	s_and_b32 s3, s3, 28
	s_ashr_i32 s4, s2, 6
	s_add_i32 s34, s3, s4
	s_ashr_i32 s6, s34, 1
	v_mov_b32_e32 v2, v0
	s_lshl_b32 s4, s6, 4
	s_ashr_i32 s5, s4, 31
	v_ashrrev_i32_e32 v3, 31, v2
	s_waitcnt lgkmcnt(0)
	v_lshl_add_u64 v[4:5], v[2:3], 2, s[10:11]
	s_lshl_b64 s[10:11], s[4:5], 11
	v_lshl_add_u64 v[6:7], v[4:5], 0, s[10:11]
	s_or_b32 s10, s4, 1
	s_ashr_i32 s11, s10, 31
	s_lshl_b64 s[10:11], s[10:11], 11
	v_lshl_add_u64 v[8:9], v[4:5], 0, s[10:11]
	s_or_b32 s10, s4, 2
	s_ashr_i32 s11, s10, 31
	s_lshl_b64 s[10:11], s[10:11], 11
	v_lshl_add_u64 v[10:11], v[4:5], 0, s[10:11]
	s_or_b32 s10, s4, 3
	s_ashr_i32 s11, s10, 31
	s_lshl_b64 s[10:11], s[10:11], 11
	v_lshl_add_u64 v[12:13], v[4:5], 0, s[10:11]
	s_or_b32 s10, s4, 4
	s_ashr_i32 s11, s10, 31
	s_lshl_b64 s[10:11], s[10:11], 11
	v_lshl_add_u64 v[14:15], v[4:5], 0, s[10:11]
	s_or_b32 s10, s4, 5
	s_ashr_i32 s11, s10, 31
	s_lshl_b64 s[10:11], s[10:11], 11
	v_lshl_add_u64 v[16:17], v[4:5], 0, s[10:11]
	s_or_b32 s10, s4, 6
	s_ashr_i32 s11, s10, 31
	s_lshl_b64 s[10:11], s[10:11], 11
	v_lshl_add_u64 v[18:19], v[4:5], 0, s[10:11]
	s_or_b32 s10, s4, 7
	s_ashr_i32 s11, s10, 31
	s_lshl_b64 s[10:11], s[10:11], 11
	v_lshl_add_u64 v[20:21], v[4:5], 0, s[10:11]
	s_or_b32 s10, s4, 8
	s_ashr_i32 s11, s10, 31
	s_lshl_b64 s[10:11], s[10:11], 11
	global_load_dword v1, v[6:7], off
	global_load_dword v3, v[8:9], off
	global_load_dword v22, v[10:11], off
	global_load_dword v23, v[12:13], off
	global_load_dword v24, v[14:15], off
	global_load_dword v25, v[16:17], off
	global_load_dword v26, v[18:19], off
	global_load_dword v27, v[20:21], off
	v_lshl_add_u64 v[6:7], v[4:5], 0, s[10:11]
	s_or_b32 s10, s4, 9
	s_ashr_i32 s11, s10, 31
	s_lshl_b64 s[10:11], s[10:11], 11
	v_lshl_add_u64 v[8:9], v[4:5], 0, s[10:11]
	s_or_b32 s10, s4, 10
	s_ashr_i32 s11, s10, 31
	s_lshl_b64 s[10:11], s[10:11], 11
	v_lshl_add_u64 v[10:11], v[4:5], 0, s[10:11]
	s_or_b32 s10, s4, 11
	s_ashr_i32 s11, s10, 31
	s_lshl_b64 s[10:11], s[10:11], 11
	v_lshl_add_u64 v[12:13], v[4:5], 0, s[10:11]
	s_or_b32 s10, s4, 12
	s_ashr_i32 s11, s10, 31
	s_lshl_b64 s[10:11], s[10:11], 11
	v_lshl_add_u64 v[14:15], v[4:5], 0, s[10:11]
	s_or_b32 s10, s4, 13
	s_ashr_i32 s11, s10, 31
	s_lshl_b64 s[10:11], s[10:11], 11
	v_lshl_add_u64 v[16:17], v[4:5], 0, s[10:11]
	s_or_b32 s10, s4, 14
	s_or_b32 s4, s4, 15
	s_ashr_i32 s11, s10, 31
	s_ashr_i32 s5, s4, 31
	s_lshl_b64 s[10:11], s[10:11], 11
	s_lshl_b64 s[4:5], s[4:5], 11
	v_lshl_add_u64 v[18:19], v[4:5], 0, s[10:11]
	v_lshl_add_u64 v[4:5], v[4:5], 0, s[4:5]
	global_load_dword v20, v[6:7], off
	global_load_dword v21, v[8:9], off
	global_load_dword v28, v[10:11], off
	global_load_dword v29, v[12:13], off
	global_load_dword v30, v[14:15], off
	global_load_dword v31, v[16:17], off
	global_load_dword v32, v[18:19], off
	global_load_dword v33, v[4:5], off
	v_lshlrev_b32_e32 v4, 3, v2
	v_ashrrev_i32_e32 v5, 31, v4
	v_lshl_add_u64 v[12:13], v[4:5], 2, s[12:13]
	global_load_dwordx4 v[4:7], v[12:13], off
	global_load_dwordx4 v[8:11], v[12:13], off offset:16
	v_and_b32_e32 v200, 63, v0
	v_lshrrev_b32_e32 v201, 6, v0
	v_lshlrev_b32_e32 v202, 4, v200
	v_and_b32_e32 v203, 32, v200
	v_xor_b32_e32 v202, v202, v203
	v_lshrrev_b32_e32 v203, 6, v202
	v_lshrrev_b32_e32 v204, 1, v201
	v_lshl_add_u32 v203, v204, 4, v203
	v_and_b32_e32 v204, 62, v202
	v_and_b32_e32 v205, 1, v201
	v_lshl_add_u32 v204, v205, 6, v204
	v_lshl_add_u32 v200, v203, 12, v204
	v_add_u32_e32 v201, 0x40000, v200
	s_lshl_b32 s72, s6, 22
	s_lshr_b32 s73, s2, 4
	s_and_b32 s73, s73, 3
	s_lshl_b32 s73, s73, 20
	s_add_u32 s72, s72, s73
	s_add_u32 s74, s70, s72
	s_addc_u32 s75, s71, 0
	s_add_u32 s76, s74, 0x80000
	s_addc_u32 s77, s75, 0
	v_readfirstlane_b32 s78, v0
	s_lshl_b32 s78, s78, 4
	s_mov_b32 m0, s78
	s_add_i32 s79, s78, 0x2000
	global_load_lds_dwordx4 v200, s[74:75]
	s_mov_b32 m0, s79
	s_add_i32 s79, s78, 0x4000
	global_load_lds_dwordx4 v201, s[74:75]
	s_mov_b32 m0, s79
	s_add_i32 s79, s78, 0x6000
	global_load_lds_dwordx4 v200, s[76:77]
	s_mov_b32 m0, s79
	s_nop 0
	global_load_lds_dwordx4 v201, s[76:77]
	s_waitcnt vmcnt(21)
	v_add_f32_e32 v1, 0, v1
	s_waitcnt vmcnt(20)
	v_add_f32_e32 v1, v1, v3
	s_waitcnt vmcnt(19)
	v_add_f32_e32 v1, v1, v22
	s_waitcnt vmcnt(18)
	v_add_f32_e32 v1, v1, v23
	s_waitcnt vmcnt(17)
	v_add_f32_e32 v1, v1, v24
	s_waitcnt vmcnt(16)
	v_add_f32_e32 v1, v1, v25
	s_waitcnt vmcnt(15)
	v_add_f32_e32 v1, v1, v26
	s_waitcnt vmcnt(14)
	v_add_f32_e32 v1, v1, v27
	s_waitcnt vmcnt(13)
	v_add_f32_e32 v1, v1, v20
	s_waitcnt vmcnt(12)
	v_add_f32_e32 v1, v1, v21
	s_waitcnt vmcnt(11)
	v_add_f32_e32 v1, v1, v28
	s_waitcnt vmcnt(10)
	v_add_f32_e32 v1, v1, v29
	s_waitcnt vmcnt(9)
	v_add_f32_e32 v1, v1, v30
	s_waitcnt vmcnt(8)
	v_add_f32_e32 v1, v1, v31
	s_waitcnt vmcnt(7)
	v_add_f32_e32 v1, v1, v32
	s_waitcnt vmcnt(6)
	v_add_f32_e32 v1, v1, v33
	v_mul_f32_e32 v12, 0x3a800000, v1
	v_mbcnt_lo_u32_b32 v1, -1, 0
	v_mbcnt_hi_u32_b32 v3, -1, v1
	v_and_b32_e32 v1, 64, v3
	v_add_u32_e32 v13, 64, v1
	v_xor_b32_e32 v1, 32, v3
	v_cmp_lt_i32_e32 vcc, v1, v13
	v_xor_b32_e32 v14, 4, v3
	s_nop 0
	v_cndmask_b32_e32 v1, v3, v1, vcc
	v_lshlrev_b32_e32 v183, 2, v1
	v_xor_b32_e32 v1, 16, v3
	v_cmp_lt_i32_e32 vcc, v1, v13
	s_nop 1
	v_cndmask_b32_e32 v1, v3, v1, vcc
	v_lshlrev_b32_e32 v181, 2, v1
	v_xor_b32_e32 v1, 8, v3
	v_cmp_lt_i32_e32 vcc, v1, v13
	s_nop 1
	v_cndmask_b32_e32 v1, v3, v1, vcc
	v_cmp_lt_i32_e32 vcc, v14, v13
	v_lshlrev_b32_e32 v1, 2, v1
	s_nop 0
	v_cndmask_b32_e32 v16, v3, v14, vcc
	s_waitcnt vmcnt(5)
	v_pk_mul_f32 v[14:15], v[12:13], v[4:5] op_sel_hi:[0,1]
	ds_bpermute_b32 v14, v183, v14
	ds_bpermute_b32 v15, v183, v15
	v_lshlrev_b32_e32 v180, 2, v16
	v_xor_b32_e32 v16, 2, v3
	v_cmp_lt_i32_e32 vcc, v16, v13
	s_waitcnt lgkmcnt(0)
	v_pk_fma_f32 v[4:5], v[12:13], v[4:5], v[14:15] op_sel_hi:[0,1,1]
	v_cndmask_b32_e32 v18, v3, v16, vcc
	v_pk_mul_f32 v[16:17], v[12:13], v[6:7] op_sel_hi:[0,1]
	ds_bpermute_b32 v14, v181, v4
	ds_bpermute_b32 v15, v181, v5
	ds_bpermute_b32 v16, v183, v16
	ds_bpermute_b32 v17, v183, v17
	v_lshlrev_b32_e32 v182, 2, v18
	v_xor_b32_e32 v18, 1, v3
	s_waitcnt lgkmcnt(2)
	v_pk_add_f32 v[4:5], v[4:5], v[14:15]
	ds_bpermute_b32 v14, v1, v4
	s_waitcnt lgkmcnt(1)
	v_pk_fma_f32 v[6:7], v[12:13], v[6:7], v[16:17] op_sel_hi:[0,1,1]
	ds_bpermute_b32 v15, v1, v5
	ds_bpermute_b32 v16, v181, v6
	ds_bpermute_b32 v17, v181, v7
	v_cmp_lt_i32_e32 vcc, v18, v13
	s_waitcnt lgkmcnt(2)
	v_pk_add_f32 v[4:5], v[4:5], v[14:15]
	ds_bpermute_b32 v14, v180, v4
	s_waitcnt lgkmcnt(1)
	v_pk_add_f32 v[6:7], v[6:7], v[16:17]
	ds_bpermute_b32 v15, v180, v5
	ds_bpermute_b32 v16, v1, v6
	ds_bpermute_b32 v17, v1, v7
	v_cndmask_b32_e32 v3, v3, v18, vcc
	v_lshlrev_b32_e32 v184, 2, v3
	s_waitcnt lgkmcnt(2)
	v_pk_add_f32 v[4:5], v[4:5], v[14:15]
	ds_bpermute_b32 v14, v182, v4
	s_waitcnt lgkmcnt(1)
	v_pk_add_f32 v[16:17], v[6:7], v[16:17]
	ds_bpermute_b32 v15, v182, v5
	ds_bpermute_b32 v18, v180, v16
	ds_bpermute_b32 v19, v180, v17
	v_and_b32_e32 v3, 63, v2
	v_cmp_eq_u32_e32 vcc, 0, v3
	s_waitcnt lgkmcnt(2)
	v_pk_add_f32 v[4:5], v[4:5], v[14:15]
	ds_bpermute_b32 v6, v184, v4
	s_waitcnt lgkmcnt(1)
	v_pk_add_f32 v[14:15], v[16:17], v[18:19]
	s_waitcnt vmcnt(4)
	v_pk_mul_f32 v[16:17], v[12:13], v[8:9] op_sel_hi:[0,1]
	v_pk_mul_f32 v[18:19], v[12:13], v[10:11] op_sel_hi:[0,1]
	ds_bpermute_b32 v16, v183, v16
	ds_bpermute_b32 v17, v183, v17
	ds_bpermute_b32 v18, v183, v18
	ds_bpermute_b32 v19, v183, v19
	ds_bpermute_b32 v20, v182, v14
	ds_bpermute_b32 v21, v182, v15
	s_waitcnt lgkmcnt(4)
	v_pk_fma_f32 v[8:9], v[12:13], v[8:9], v[16:17] op_sel_hi:[0,1,1]
	ds_bpermute_b32 v16, v181, v8
	s_waitcnt lgkmcnt(3)
	v_pk_fma_f32 v[10:11], v[12:13], v[10:11], v[18:19] op_sel_hi:[0,1,1]
	ds_bpermute_b32 v17, v181, v9
	ds_bpermute_b32 v12, v181, v10
	ds_bpermute_b32 v13, v181, v11
	ds_bpermute_b32 v7, v184, v5
	s_waitcnt lgkmcnt(3)
	v_pk_add_f32 v[16:17], v[8:9], v[16:17]
	ds_bpermute_b32 v18, v1, v16
	s_waitcnt lgkmcnt(2)
	v_pk_add_f32 v[10:11], v[10:11], v[12:13]
	ds_bpermute_b32 v19, v1, v17
	ds_bpermute_b32 v12, v1, v10
	ds_bpermute_b32 v13, v1, v11
	v_pk_add_f32 v[8:9], v[14:15], v[20:21]
	s_waitcnt lgkmcnt(2)
	v_pk_add_f32 v[14:15], v[16:17], v[18:19]
	ds_bpermute_b32 v16, v180, v14
	s_waitcnt lgkmcnt(1)
	v_pk_add_f32 v[12:13], v[10:11], v[12:13]
	ds_bpermute_b32 v17, v180, v15
	ds_bpermute_b32 v18, v180, v12
	ds_bpermute_b32 v19, v180, v13
	ds_bpermute_b32 v10, v184, v8
	ds_bpermute_b32 v11, v184, v9
	s_waitcnt lgkmcnt(4)
	v_pk_add_f32 v[14:15], v[14:15], v[16:17]
	ds_bpermute_b32 v16, v182, v14
	s_waitcnt lgkmcnt(3)
	v_pk_add_f32 v[18:19], v[12:13], v[18:19]
	ds_bpermute_b32 v17, v182, v15
	ds_bpermute_b32 v20, v182, v18
	ds_bpermute_b32 v21, v182, v19
	s_waitcnt lgkmcnt(2)
	v_pk_add_f32 v[12:13], v[14:15], v[16:17]
	ds_bpermute_b32 v14, v184, v12
	s_waitcnt lgkmcnt(1)
	v_pk_add_f32 v[16:17], v[18:19], v[20:21]
	ds_bpermute_b32 v15, v184, v13
	ds_bpermute_b32 v18, v184, v16
	ds_bpermute_b32 v19, v184, v17
	s_and_saveexec_b64 s[4:5], vcc
	s_cbranch_execz .LBB5_2
	v_ashrrev_i32_e32 v2, 1, v2
	v_add_u32_e32 v2, 0, v2
	v_add_u32_e32 v20, 0x20000, v2
	v_pk_add_f32 v[2:3], v[4:5], v[6:7]
	ds_write2_b32 v20, v2, v3 offset1:1
	v_pk_add_f32 v[2:3], v[8:9], v[10:11]
	ds_write2_b32 v20, v2, v3 offset0:2 offset1:3
	s_waitcnt lgkmcnt(4)
	v_pk_add_f32 v[2:3], v[12:13], v[14:15]
	ds_write2_b32 v20, v2, v3 offset0:4 offset1:5
	s_waitcnt lgkmcnt(3)
	v_pk_add_f32 v[2:3], v[16:17], v[18:19]
	ds_write2_b32 v20, v2, v3 offset0:6 offset1:7

.LBB5_6:
	s_or_b64 exec, exec, s[10:11]
	s_load_dwordx2 s[10:11], s[0:1], 0x80
	s_load_dwordx2 s[36:37], s[0:1], 0x70
	s_load_dwordx2 s[40:41], s[0:1], 0x60
	s_load_dwordx4 s[20:23], s[0:1], 0x50
	s_load_dwordx8 s[12:19], s[0:1], 0x30
	s_load_dwordx4 s[24:27], s[0:1], 0x10
	s_load_dwordx2 s[46:47], s[0:1], 0x20
	s_and_b32 s58, s59, 1
	s_cmp_eq_u32 s35, 0
	s_cselect_b32 s42, s3, s7
	s_ashr_i32 s7, s6, 31
	s_lshl_b64 s[52:53], s[6:7], 22
	s_waitcnt lgkmcnt(0)
	s_lshl_b32 s64, s42, 11
	s_lshl_b32 s65, s58, 10
	s_add_u32 s64, s64, s65
	s_add_u32 s66, s24, s64
	s_addc_u32 s67, s25, 0
	s_mov_b32 m0, 0x22240
	v_and_b32_e32 v254, 63, v0
	v_lshlrev_b32_e32 v254, 4, v254
	global_load_lds_dwordx4 v254, s[66:67]
	s_lshl_b32 s64, s42, 10
	s_add_u32 s66, s12, s64
	s_addc_u32 s67, s13, 0
	s_mov_b32 m0, 0x22640
	s_lshl_b32 s65, s42, 2
	global_load_lds_dwordx4 v254, s[66:67]
	s_add_u32 s66, s14, s64
	s_addc_u32 s67, s15, 0
	s_mov_b32 m0, 0x22a40
	s_nop 0
	global_load_lds_dwordx4 v254, s[66:67]
	s_add_u32 s66, s16, s64
	s_addc_u32 s67, s17, 0
	s_mov_b32 m0, 0x22e40
	s_load_dword s69, s[18:19], s65
	global_load_lds_dwordx4 v254, s[66:67]
	s_add_u32 s3, s28, s52
	s_addc_u32 s7, s29, s53
	s_lshl_b32 s35, s33, 19
	s_and_b32 s35, s35, 0x300000
	s_add_u32 s50, s3, s35
	s_addc_u32 s51, s7, 0
	s_ashr_i32 s43, s42, 31
	s_lshl_b32 s7, s58, 8
	s_lshl_b64 s[54:55], s[42:43], 21
	v_lshlrev_b32_e32 v162, 4, v0
	v_and_b32_e32 v2, 32, v0
	s_add_u32 s35, s30, s54
	v_bitop3_b32 v12, v162, v2, 48 bitop3:0x6c
	v_and_b32_e32 v13, 64, v0
	s_addc_u32 s38, s31, s55
	s_lshl_b32 s3, s58, 20
	v_lshrrev_b32_e32 v4, 3, v0
	v_bfe_u32 v3, v0, 2, 4
	v_or_b32_e32 v2, v12, v13
	v_or_b32_e32 v164, 0x2000, v162
	s_add_u32 s56, s35, s3
	v_and_or_b32 v4, v4, 48, v3
	v_lshrrev_b32_e32 v2, 1, v2
	v_lshrrev_b32_e32 v5, 7, v164
	s_movk_i32 s35, 0x70
	v_add_u32_e32 v142, 0, v162
	v_lshl_or_b32 v4, v4, 11, v2
	v_and_or_b32 v5, v5, s35, v3
	v_readfirstlane_b32 s35, v142
	v_add_u32_e32 v143, 0x2000, v142
	v_lshlrev_b32_e32 v130, 1, v4
	s_mov_b32 m0, s35
	v_readfirstlane_b32 s35, v143
	s_addc_u32 s57, s38, 0
	s_mov_b32 m0, s35
	s_add_i32 s35, 0, 0x10000
	v_lshl_or_b32 v2, v5, 11, v2
	v_add_u32_e32 v144, s35, v162
	v_lshlrev_b32_e32 v132, 1, v2
	v_readfirstlane_b32 s38, v144
	v_add_u32_e32 v145, 0x2000, v144
	s_mov_b32 m0, s38
	v_readfirstlane_b32 s38, v145
	v_add_u32_e32 v151, 0x4000, v142
	global_load_lds_dwordx4 v130, s[56:57]
	s_mov_b32 m0, s38
	s_add_u32 s38, s50, 0x80000
	v_readfirstlane_b32 s44, v151
	v_add_u32_e32 v153, 0x6000, v142
	global_load_lds_dwordx4 v132, s[56:57]
	s_addc_u32 s39, s51, 0
	s_mov_b32 m0, s44
	v_readfirstlane_b32 s44, v153
	s_mov_b32 m0, s44
	v_mov_b32_e32 v2, 0
	s_add_u32 s38, s56, 0x80000
	s_addc_u32 s39, s57, 0
	s_add_i32 s60, 0, 0x14000
	v_add_u32_e32 v154, s60, v162
	v_add_u32_e32 v155, 0x2000, v154
	v_readfirstlane_b32 s44, v154
	s_mov_b32 m0, s44
	v_readfirstlane_b32 s44, v155
	global_load_lds_dwordx4 v130, s[38:39]
	s_mov_b32 m0, s44
	v_lshrrev_b32_e32 v14, 8, v0
	global_load_lds_dwordx4 v132, s[38:39]
	v_mov_b32_e32 v131, v2
	v_mov_b32_e32 v133, v2
	v_lshl_add_u64 v[10:11], s[50:51], 0, v[130:131]
	v_lshl_add_u64 v[8:9], s[50:51], 0, v[132:133]
	v_lshl_add_u64 v[6:7], s[56:57], 0, v[130:131]
	v_lshl_add_u64 v[4:5], s[56:57], 0, v[132:133]
	v_cmp_eq_u32_e32 vcc, 1, v14
	s_and_saveexec_b64 s[38:39], vcc
	s_cbranch_execz .LBB5_8
	s_barrier
.LBB5_8:
	s_or_b64 exec, exec, s[38:39]
	v_add_u32_e32 v156, 0x8000, v142
	s_load_dwordx2 s[38:39], s[0:1], 0x78
	s_load_dwordx2 s[44:45], s[0:1], 0x68
	s_load_dwordx2 s[48:49], s[0:1], 0x28
	s_mov_b64 s[0:1], 0x80
	v_readfirstlane_b32 s61, v156
	v_add_u32_e32 v157, 0xa000, v142
	v_lshl_add_u64 v[10:11], v[10:11], 0, s[0:1]
	s_mov_b32 m0, s61
	v_readfirstlane_b32 s61, v157
	s_waitcnt vmcnt(2)
	s_barrier
	global_load_lds_dwordx4 v[10:11], off
	s_mov_b32 m0, s61
	s_add_i32 s61, 0, 0x18000
	v_add_u32_e32 v158, s61, v162
	v_lshl_add_u64 v[8:9], v[8:9], 0, s[0:1]
	v_readfirstlane_b32 s62, v158
	s_add_u32 s56, s56, 0x80080
	global_load_lds_dwordx4 v[8:9], off
	s_mov_b32 m0, s62
	v_add_u32_e32 v159, 0x2000, v158
	s_addc_u32 s57, s57, 0
	s_add_i32 s62, 0, 0x1c000
	v_lshl_add_u64 v[6:7], v[6:7], 0, s[0:1]
	v_lshl_add_u64 v[4:5], v[4:5], 0, s[0:1]
	v_readfirstlane_b32 s0, v159
	v_add_u32_e32 v160, s62, v162
	global_load_lds_dwordx4 v[6:7], off
	s_mov_b32 m0, s0
	v_readfirstlane_b32 s63, v160
	v_add_u32_e32 v161, 0x2000, v160
	global_load_lds_dwordx4 v[4:5], off
	s_mov_b32 m0, s63
	v_readfirstlane_b32 s63, v161
	global_load_lds_dwordx4 v130, s[56:57]
	s_mov_b32 m0, s63
	v_lshlrev_b32_e32 v4, 6, v0
	global_load_lds_dwordx4 v132, s[56:57]
	v_lshlrev_b32_e32 v185, 2, v0
	v_and_b32_e32 v146, 48, v0
	v_and_b32_e32 v5, 0x3c0, v4
	v_and_b32_e32 v152, 32, v185
	v_bitop3_b32 v5, v5, v152, v146 bitop3:0x36
	s_add_u32 s3, s54, s3
	v_add_u32_e32 v8, s35, v5
	s_addc_u32 s35, s55, 0
	s_add_u32 s30, s30, s3
	s_addc_u32 s31, s31, s35
	s_lshl_b32 s2, s2, 16
	v_and_b32_e32 v15, 0x3000, v4
	v_add_u16_e32 v4, v12, v13
	s_and_b32 s2, s2, 0x300000
	v_lshrrev_b16_e32 v6, 1, v4
	v_lshlrev_b32_e32 v4, 8, v0
	v_lshlrev_b32_e32 v7, 4, v164
	s_add_u32 s2, s52, s2
	v_and_b32_e32 v4, 0x18000, v4
	v_lshlrev_b32_e32 v3, 11, v3
	v_and_b32_e32 v7, 0x38000, v7
	s_addc_u32 s3, s53, 0
	s_waitcnt vmcnt(6)
	v_lshlrev_b32_e32 v14, 13, v14
	v_or3_b32 v4, v6, v4, v3
	v_or3_b32 v3, v6, v7, v3
	s_add_u32 s2, s28, s2
	v_add_u32_e32 v9, s60, v5
	v_add_u32_e32 v10, s61, v5
	v_add_u32_e32 v11, s62, v5
	v_add_u32_e32 v16, 0, v5
	v_or_b32_e32 v17, 0x800, v14
	v_or_b32_e32 v18, 0x1000, v14
	v_or_b32_e32 v19, 0x1800, v14
	v_lshlrev_b32_e32 v4, 1, v4
	v_mov_b32_e32 v5, v2
	v_lshlrev_b32_e32 v6, 1, v3
	v_mov_b32_e32 v7, v2
	s_addc_u32 s3, s29, s3
	s_mov_b64 s[0:1], 0x80080
	v_lshl_add_u64 v[134:135], s[30:31], 0, v[4:5]
	v_lshl_add_u64 v[136:137], s[30:31], 0, v[6:7]
	v_lshl_add_u64 v[138:139], s[2:3], 0, v[4:5]
	v_lshl_add_u64 v[140:141], s[2:3], 0, v[6:7]
	s_mov_b32 s35, -2
	s_mov_b64 s[2:3], 0
	v_add_u32_e32 v165, v8, v15
	v_add_u32_e32 v150, v16, v14
	v_add_u32_e32 v149, v16, v17
	v_add_u32_e32 v148, v16, v18
	v_add_u32_e32 v147, v16, v19
	v_add_u32_e32 v163, v9, v15
	s_mov_b64 s[28:29], 0x100
	s_mov_b64 s[30:31], 0x80100
	v_add_u32_e32 v133, v10, v15
	s_mov_b64 s[52:53], 0x180
	s_mov_b64 s[54:55], 0x80180
	v_add_u32_e32 v131, v11, v15
	v_mov_b32_e32 v3, v2
	v_mov_b32_e32 v4, v2
	v_mov_b32_e32 v6, v2
	v_mov_b32_e32 v8, v2
	v_mov_b32_e32 v9, v2
	v_mov_b32_e32 v10, v2
	v_mov_b32_e32 v11, v2
	v_mov_b32_e32 v12, v2
	v_mov_b32_e32 v13, v2
	v_mov_b32_e32 v14, v2
	v_mov_b32_e32 v15, v2
	v_mov_b32_e32 v16, v2
	v_mov_b32_e32 v17, v2
	v_mov_b32_e32 v18, v2
	v_mov_b32_e32 v19, v2
	v_mov_b32_e32 v20, v2
	v_mov_b32_e32 v21, v2
	v_mov_b32_e32 v22, v2
	v_mov_b32_e32 v23, v2
	v_mov_b32_e32 v24, v2
	v_mov_b32_e32 v25, v2
	v_mov_b32_e32 v26, v2
	v_mov_b32_e32 v27, v2
	v_mov_b32_e32 v28, v2
	v_mov_b32_e32 v29, v2
	v_mov_b32_e32 v30, v2
	v_mov_b32_e32 v31, v2
	v_mov_b32_e32 v32, v2
	v_mov_b32_e32 v33, v2
	v_mov_b32_e32 v34, v2
	v_mov_b32_e32 v35, v2
	v_mov_b32_e32 v36, v2
	v_mov_b32_e32 v37, v2
	v_mov_b32_e32 v38, v2
	v_mov_b32_e32 v39, v2
	v_mov_b32_e32 v40, v2
	v_mov_b32_e32 v41, v2
	v_mov_b32_e32 v42, v2
	v_mov_b32_e32 v43, v2
	v_mov_b32_e32 v44, v2
	v_mov_b32_e32 v45, v2
	v_mov_b32_e32 v46, v2
	v_mov_b32_e32 v47, v2
	v_mov_b32_e32 v48, v2
	v_mov_b32_e32 v49, v2
	v_mov_b32_e32 v50, v2
	v_mov_b32_e32 v51, v2
	v_mov_b32_e32 v52, v2
	v_mov_b32_e32 v53, v2
	v_mov_b32_e32 v54, v2
	v_mov_b32_e32 v55, v2
	v_mov_b32_e32 v56, v2
	v_mov_b32_e32 v57, v2
	v_mov_b32_e32 v58, v2
	v_mov_b32_e32 v59, v2
	v_mov_b32_e32 v60, v2
	v_mov_b32_e32 v61, v2
	v_mov_b32_e32 v62, v2
	v_mov_b32_e32 v63, v2
	v_mov_b32_e32 v64, v2
	v_mov_b32_e32 v65, v2
	v_mov_b32_e32 v66, v2
	v_mov_b32_e32 v67, v2
	v_mov_b32_e32 v68, v2
	v_mov_b32_e32 v69, v2
	v_mov_b32_e32 v70, v2
	v_mov_b32_e32 v71, v2
	v_mov_b32_e32 v72, v2
	v_mov_b32_e32 v73, v2
	v_mov_b32_e32 v74, v2
	v_mov_b32_e32 v75, v2
	v_mov_b32_e32 v76, v2
	v_mov_b32_e32 v77, v2
	v_mov_b32_e32 v78, v2
	v_mov_b32_e32 v79, v2
	v_mov_b32_e32 v80, v2
	v_mov_b32_e32 v81, v2
	v_mov_b32_e32 v82, v2
	v_mov_b32_e32 v83, v2
	v_mov_b32_e32 v84, v2
	v_mov_b32_e32 v85, v2
	v_mov_b32_e32 v86, v2
	v_mov_b32_e32 v87, v2
	v_mov_b32_e32 v88, v2
	v_mov_b32_e32 v89, v2
	v_mov_b32_e32 v90, v2
	v_mov_b32_e32 v91, v2
	v_mov_b32_e32 v92, v2
	v_mov_b32_e32 v93, v2
	v_mov_b32_e32 v94, v2
	v_mov_b32_e32 v95, v2
	v_mov_b32_e32 v96, v2
	v_mov_b32_e32 v97, v2
	v_mov_b32_e32 v98, v2
	v_mov_b32_e32 v99, v2
	v_mov_b32_e32 v100, v2
	v_mov_b32_e32 v101, v2
	v_mov_b32_e32 v102, v2
	v_mov_b32_e32 v103, v2
	v_mov_b32_e32 v104, v2
	v_mov_b32_e32 v105, v2
	v_mov_b32_e32 v106, v2
	v_mov_b32_e32 v107, v2
	v_mov_b32_e32 v108, v2
	v_mov_b32_e32 v109, v2
	v_mov_b32_e32 v110, v2
	v_mov_b32_e32 v111, v2
	v_mov_b32_e32 v112, v2
	v_mov_b32_e32 v113, v2
	v_mov_b32_e32 v114, v2
	v_mov_b32_e32 v115, v2
	v_mov_b32_e32 v116, v2
	v_mov_b32_e32 v117, v2
	v_mov_b32_e32 v118, v2
	v_mov_b32_e32 v119, v2
	v_mov_b32_e32 v120, v2
	v_mov_b32_e32 v121, v2
	v_mov_b32_e32 v122, v2
	v_mov_b32_e32 v123, v2
	v_mov_b32_e32 v124, v2
	v_mov_b32_e32 v125, v2
	v_mov_b32_e32 v126, v2
	v_mov_b32_e32 v127, v2
	v_mov_b32_e32 v128, v2
	v_mov_b32_e32 v129, v2
	v_lshrrev_b32_e32 v190, 2, v0
	v_and_b32_e32 v186, 48, v162
	v_and_b32_e32 v188, 15, v0
	v_add_u32_e32 v166, 0xc000, v142
	v_add_u32_e32 v167, 0xe000, v142
	s_barrier

	.amdhsa_kernel _Z8k_expertPKDF16_S0_PKfPcPiS0_S2_S2_S2_S2_PfS5_S4_S2_S2_S2_S2_S5_S2_S2_S2_
		.amdhsa_group_segment_fixed_size 0
		.amdhsa_private_segment_fixed_size 0
		.amdhsa_kernarg_size 168
		.amdhsa_user_sgpr_count 2
		.amdhsa_user_sgpr_dispatch_ptr 0
		.amdhsa_user_sgpr_queue_ptr 0
		.amdhsa_user_sgpr_kernarg_segment_ptr 1
		.amdhsa_user_sgpr_dispatch_id 0
		.amdhsa_user_sgpr_kernarg_preload_length 0
		.amdhsa_user_sgpr_kernarg_preload_offset 0
		.amdhsa_user_sgpr_private_segment_size 0
		.amdhsa_uses_dynamic_stack 0
		.amdhsa_enable_private_segment 0
		.amdhsa_system_sgpr_workgroup_id_x 1
		.amdhsa_system_sgpr_workgroup_id_y 0
		.amdhsa_system_sgpr_workgroup_id_z 0
		.amdhsa_system_sgpr_workgroup_info 0
		.amdhsa_system_vgpr_workitem_id 0
		.amdhsa_next_free_vgpr 256
		.amdhsa_next_free_sgpr 80
		.amdhsa_accum_offset 256
		.amdhsa_reserve_vcc 1
		.amdhsa_float_round_mode_32 0
		.amdhsa_float_round_mode_16_64 0
		.amdhsa_float_denorm_mode_32 3
		.amdhsa_float_denorm_mode_16_64 3
		.amdhsa_dx10_clamp 1
		.amdhsa_ieee_mode 1
		.amdhsa_fp16_overflow 0
		.amdhsa_tg_split 0
		.amdhsa_exception_fp_ieee_invalid_op 0
		.amdhsa_exception_fp_denorm_src 0
		.amdhsa_exception_fp_ieee_div_zero 0
		.amdhsa_exception_fp_ieee_overflow 0
		.amdhsa_exception_fp_ieee_underflow 0
		.amdhsa_exception_fp_ieee_inexact 0
		.amdhsa_exception_int_div_zero 0
	.end_amdhsa_kernel

amdhsa.kernels:
  - .agpr_count:     0
    .args:
      - .actual_access:  read_only
        .address_space:  global
        .offset:         0
        .size:           8
        .value_kind:     global_buffer
      - .actual_access:  read_only
        .address_space:  global
        .offset:         8
        .size:           8
        .value_kind:     global_buffer
      - .actual_access:  read_only
        .address_space:  global
        .offset:         16
        .size:           8
        .value_kind:     global_buffer
      - .actual_access:  write_only
        .address_space:  global
        .offset:         24
        .size:           8
        .value_kind:     global_buffer
      - .actual_access:  write_only
        .address_space:  global
        .offset:         32
        .size:           8
        .value_kind:     global_buffer
      - .actual_access:  read_only
        .address_space:  global
        .offset:         40
        .size:           8
        .value_kind:     global_buffer
      - .actual_access:  read_only
        .address_space:  global
        .offset:         48
        .size:           8
        .value_kind:     global_buffer
      - .actual_access:  read_only
        .address_space:  global
        .offset:         56
        .size:           8
        .value_kind:     global_buffer
      - .actual_access:  read_only
        .address_space:  global
        .offset:         64
        .size:           8
        .value_kind:     global_buffer
      - .actual_access:  read_only
        .address_space:  global
        .offset:         72
        .size:           8
        .value_kind:     global_buffer
      - .actual_access:  read_only
        .address_space:  global
        .offset:         80
        .size:           8
        .value_kind:     global_buffer
    .group_segment_fixed_size: 16384
    .kernarg_segment_align: 8
    .kernarg_segment_size: 88
    .language:       OpenCL C
    .language_version:
      - 2
      - 0
    .max_flat_workgroup_size: 768
    .name:           _Z9k_router2PKfPKDF16_S0_PDF16_PfPiS0_S0_S4_S5_S4_
    .private_segment_fixed_size: 0
    .sgpr_count:     21
    .sgpr_spill_count: 0
    .symbol:         _Z9k_router2PKfPKDF16_S0_PDF16_PfPiS0_S0_S4_S5_S4_.kd
    .uniform_work_group_size: 1
    .uses_dynamic_stack: false
    .vgpr_count:     168
    .vgpr_spill_count: 0
    .wavefront_size: 64
  - .agpr_count:     0
    .args:
      - .actual_access:  read_only
        .address_space:  global
        .offset:         0
        .size:           8
        .value_kind:     global_buffer
      - .actual_access:  read_only
        .address_space:  global
        .offset:         8
        .size:           8
        .value_kind:     global_buffer
      - .actual_access:  read_only
        .address_space:  global
        .offset:         16
        .size:           8
        .value_kind:     global_buffer
      - .actual_access:  write_only
        .address_space:  global
        .offset:         24
        .size:           8
        .value_kind:     global_buffer
      - .actual_access:  write_only
        .address_space:  global
        .offset:         32
        .size:           8
        .value_kind:     global_buffer
      - .actual_access:  write_only
        .address_space:  global
        .offset:         40
        .size:           8
        .value_kind:     global_buffer
    .group_segment_fixed_size: 256
    .kernarg_segment_align: 8
    .kernarg_segment_size: 48
    .language:       OpenCL C
    .language_version:
      - 2
      - 0
    .max_flat_workgroup_size: 256
    .name:           _Z6k_gatePKfS0_S0_PfPiS1_
    .private_segment_fixed_size: 0
    .sgpr_count:     26
    .sgpr_spill_count: 0
    .symbol:         _Z6k_gatePKfS0_S0_PfPiS1_.kd
    .uniform_work_group_size: 1
    .uses_dynamic_stack: false
    .vgpr_count:     51
    .vgpr_spill_count: 0
    .wavefront_size: 64
  - .agpr_count:     0
    .args:
      - .actual_access:  read_only
        .address_space:  global
        .offset:         0
        .size:           8
        .value_kind:     global_buffer
      - .actual_access:  write_only
        .address_space:  global
        .offset:         8
        .size:           8
        .value_kind:     global_buffer
      - .actual_access:  read_only
        .address_space:  global
        .offset:         16
        .size:           8
        .value_kind:     global_buffer
      - .actual_access:  read_only
        .address_space:  global
        .offset:         24
        .size:           8
        .value_kind:     global_buffer
      - .actual_access:  read_only
        .address_space:  global
        .offset:         32
        .size:           8
        .value_kind:     global_buffer
      - .actual_access:  write_only
        .address_space:  global
        .offset:         40
        .size:           8
        .value_kind:     global_buffer
      - .actual_access:  write_only
        .address_space:  global
        .offset:         48
        .size:           8
        .value_kind:     global_buffer
      - .actual_access:  write_only
        .address_space:  global
        .offset:         56
        .size:           8
        .value_kind:     global_buffer
      - .actual_access:  write_only
        .address_space:  global
        .offset:         64
        .size:           8
        .value_kind:     global_buffer
      - .actual_access:  write_only
        .address_space:  global
        .offset:         72
        .size:           8
        .value_kind:     global_buffer
    .group_segment_fixed_size: 16640
    .kernarg_segment_align: 8
    .kernarg_segment_size: 80
    .language:       OpenCL C
    .language_version:
      - 2
      - 0
    .max_flat_workgroup_size: 256
    .name:           _Z10k_prep_allPKfPDF16_S0_S0_S0_S1_S1_PiS2_S2_
    .private_segment_fixed_size: 0
    .sgpr_count:     20
    .sgpr_spill_count: 0
    .symbol:         _Z10k_prep_allPKfPDF16_S0_S0_S0_S1_S1_PiS2_S2_.kd
    .uniform_work_group_size: 1
    .uses_dynamic_stack: false
    .vgpr_count:     37
    .vgpr_spill_count: 0
    .wavefront_size: 64
  - .agpr_count:     0
    .args:
      - .address_space:  global
        .offset:         0
        .size:           8
        .value_kind:     global_buffer
      - .address_space:  global
        .offset:         8
        .size:           8
        .value_kind:     global_buffer
      - .actual_access:  read_only
        .address_space:  global
        .offset:         16
        .size:           8
        .value_kind:     global_buffer
      - .actual_access:  read_only
        .address_space:  global
        .offset:         24
        .size:           8
        .value_kind:     global_buffer
      - .actual_access:  write_only
        .address_space:  global
        .offset:         32
        .size:           8
        .value_kind:     global_buffer
    .group_segment_fixed_size: 0
    .kernarg_segment_align: 8
    .kernarg_segment_size: 40
    .language:       OpenCL C
    .language_version:
      - 2
      - 0
    .max_flat_workgroup_size: 512
    .name:           _Z7k_gemm1PKDF16_S0_PKfPKiPDF16_
    .private_segment_fixed_size: 0
    .sgpr_count:     36
    .sgpr_spill_count: 0
    .symbol:         _Z7k_gemm1PKDF16_S0_PKfPKiPDF16_.kd
    .uniform_work_group_size: 1
    .uses_dynamic_stack: false
    .vgpr_count:     240
    .vgpr_spill_count: 0
    .wavefront_size: 64
  - .agpr_count:     0
    .args:
      - .address_space:  global
        .offset:         0
        .size:           8
        .value_kind:     global_buffer
      - .actual_access:  read_only
        .address_space:  global
        .offset:         8
        .size:           8
        .value_kind:     global_buffer
      - .actual_access:  read_only
        .address_space:  global
        .offset:         16
        .size:           8
        .value_kind:     global_buffer
      - .actual_access:  read_only
        .address_space:  global
        .offset:         24
        .size:           8
        .value_kind:     global_buffer
      - .actual_access:  read_only
        .address_space:  global
        .offset:         32
        .size:           8
        .value_kind:     global_buffer
      - .actual_access:  read_only
        .address_space:  global
        .offset:         40
        .size:           8
        .value_kind:     global_buffer
      - .actual_access:  read_only
        .address_space:  global
        .offset:         48
        .size:           8
        .value_kind:     global_buffer
      - .actual_access:  write_only
        .address_space:  global
        .offset:         56
        .size:           8
        .value_kind:     global_buffer
      - .actual_access:  write_only
        .address_space:  global
        .offset:         64
        .size:           8
        .value_kind:     global_buffer
    .group_segment_fixed_size: 0
    .kernarg_segment_align: 8
    .kernarg_segment_size: 72
    .language:       OpenCL C
    .language_version:
      - 2
      - 0
    .max_flat_workgroup_size: 512
    .name:           _Z11k_gemm2poolPKDF16_S0_PKfS2_S2_S2_PKiPfS5_
    .private_segment_fixed_size: 0
    .sgpr_count:     32
    .sgpr_spill_count: 0
    .symbol:         _Z11k_gemm2poolPKDF16_S0_PKfS2_S2_S2_PKiPfS5_.kd
    .uniform_work_group_size: 1
    .uses_dynamic_stack: false
    .vgpr_count:     198
    .vgpr_spill_count: 0
    .wavefront_size: 64
  - .agpr_count:     0
    .args:
      - .address_space:  global
        .offset:         0
        .size:           8
        .value_kind:     global_buffer
      - .address_space:  global
        .offset:         8
        .size:           8
        .value_kind:     global_buffer
      - .actual_access:  read_only
        .address_space:  global
        .offset:         16
        .size:           8
        .value_kind:     global_buffer
      - .address_space:  global
        .offset:         24
        .size:           8
        .value_kind:     global_buffer
      - .address_space:  global
        .offset:         32
        .size:           8
        .value_kind:     global_buffer
      - .actual_access:  read_only
        .address_space:  global
        .offset:         40
        .size:           8
        .value_kind:     global_buffer
      - .actual_access:  read_only
        .address_space:  global
        .offset:         48
        .size:           8
        .value_kind:     global_buffer
      - .actual_access:  read_only
        .address_space:  global
        .offset:         56
        .size:           8
        .value_kind:     global_buffer
      - .actual_access:  read_only
        .address_space:  global
        .offset:         64
        .size:           8
        .value_kind:     global_buffer
      - .actual_access:  read_only
        .address_space:  global
        .offset:         72
        .size:           8
        .value_kind:     global_buffer
      - .address_space:  global
        .offset:         80
        .size:           8
        .value_kind:     global_buffer
      - .address_space:  global
        .offset:         88
        .size:           8
        .value_kind:     global_buffer
      - .address_space:  global
        .offset:         96
        .size:           8
        .value_kind:     global_buffer
      - .actual_access:  read_only
        .address_space:  global
        .offset:         104
        .size:           8
        .value_kind:     global_buffer
      - .actual_access:  read_only
        .address_space:  global
        .offset:         112
        .size:           8
        .value_kind:     global_buffer
      - .actual_access:  read_only
        .address_space:  global
        .offset:         120
        .size:           8
        .value_kind:     global_buffer
      - .actual_access:  read_only
        .address_space:  global
        .offset:         128
        .size:           8
        .value_kind:     global_buffer
      - .actual_access:  write_only
        .address_space:  global
        .offset:         136
        .size:           8
        .value_kind:     global_buffer
      - .actual_access:  read_only
        .address_space:  global
        .offset:         144
        .size:           8
        .value_kind:     global_buffer
      - .actual_access:  read_only
        .address_space:  global
        .offset:         152
        .size:           8
        .value_kind:     global_buffer
      - .actual_access:  read_only
        .address_space:  global
        .offset:         160
        .size:           8
        .value_kind:     global_buffer
    .group_segment_fixed_size: 0
    .kernarg_segment_align: 8
    .kernarg_segment_size: 168
    .language:       OpenCL C
    .language_version:
      - 2
      - 0
    .max_flat_workgroup_size: 512
    .name:           _Z8k_expertPKDF16_S0_PKfPcPiS0_S2_S2_S2_S2_PfS5_S4_S2_S2_S2_S2_S5_S2_S2_S2_
    .private_segment_fixed_size: 0
    .sgpr_count:     86
    .sgpr_spill_count: 0
    .symbol:         _Z8k_expertPKDF16_S0_PKfPcPiS0_S2_S2_S2_S2_PfS5_S4_S2_S2_S2_S2_S5_S2_S2_S2_.kd
    .uniform_work_group_size: 1
    .uses_dynamic_stack: false
    .vgpr_count:     256
    .vgpr_spill_count: 0
    .wavefront_size: 64
  - .agpr_count:     0
    .args:
      - .actual_access:  read_only
        .address_space:  global
        .offset:         0
        .size:           8
        .value_kind:     global_buffer
      - .actual_access:  read_only
        .address_space:  global
        .offset:         8
        .size:           8
        .value_kind:     global_buffer
      - .actual_access:  read_only
        .address_space:  global
        .offset:         16
        .size:           8
        .value_kind:     global_buffer
      - .actual_access:  read_only
        .address_space:  global
        .offset:         24
        .size:           8
        .value_kind:     global_buffer
      - .actual_access:  read_only
        .address_space:  global
        .offset:         32
        .size:           8
        .value_kind:     global_buffer
      - .actual_access:  read_only
        .address_space:  global
        .offset:         40
        .size:           8
        .value_kind:     global_buffer
      - .actual_access:  read_only
        .address_space:  global
        .offset:         48
        .size:           8
        .value_kind:     global_buffer
      - .actual_access:  read_only
        .address_space:  global
        .offset:         56
        .size:           8
        .value_kind:     global_buffer
      - .actual_access:  write_only
        .address_space:  global
        .offset:         64
        .size:           8
        .value_kind:     global_buffer
    .group_segment_fixed_size: 8768
    .kernarg_segment_align: 8
    .kernarg_segment_size: 72
    .language:       OpenCL C
    .language_version:
      - 2
      - 0
    .max_flat_workgroup_size: 1024
    .name:           _Z7k_finalPKfS0_S0_S0_S0_PKiS0_S0_Pf
    .private_segment_fixed_size: 0
    .sgpr_count:     24
    .sgpr_spill_count: 0
    .symbol:         _Z7k_finalPKfS0_S0_S0_S0_PKiS0_S0_Pf.kd
    .uniform_work_group_size: 1
    .uses_dynamic_stack: false
    .vgpr_count:     83
    .vgpr_spill_count: 0
    .wavefront_size: 64
